# rider end block reordered (LDS drained and tile store issued before the four weight loads); rider start staggered by 8 trips on odd workgroups
# speedup vs baseline: 1.0039x; 1.0039x over previous
; DI void attn_unit_d8(unsigned char* lds, const AttnArgs& a) {
;     ...
;     f32x16 o0[2], o1[2];
; #pragma unroll
;     for (int d = 0; d < 2; ++d) { o0[d] = (f32x16){}; o1[d] = (f32x16){}; }
;     f32x4 l0 = {0.f, 0.f, 0.f, 0.f}, l1 = {0.f, 0.f, 0.f, 0.f};
;     ...
;     if (wid >= 4) __builtin_amdgcn_s_setprio(1);
;     int sb = 0;
;     const v8i zz8 = (v8i){0, 0, 0, 0, 0, 0, 0, 0};
;     v8i PaX = zz8, PbX = zz8, PaY = zz8, PbY = zz8, vX0 = zz8, vX1 = zz8, vY0 = zz8, vY1 = zz8;
.LBB0_662:
	s_and_b32 s61, s42, 1
	s_lshl_b32 s61, s61, 3
	s_sub_i32 s61, 0, s61
	v_mov_b32_e32 v2, 0
	s_mov_b32 s16, 0
	v_mov_b32_e32 v138, 0
	v_mov_b32_e32 v139, 0
	v_mov_b32_e32 v140, 0
	v_mov_b32_e32 v141, 0
	v_mov_b32_e32 v142, 0
	v_mov_b32_e32 v143, 0
	v_mov_b32_e32 v144, 0
	v_mov_b32_e32 v145, 0
	v_mov_b32_e32 v130, 0
	v_mov_b32_e32 v131, 0
	v_mov_b32_e32 v132, 0
	v_mov_b32_e32 v133, 0
	v_mov_b32_e32 v134, 0
	v_mov_b32_e32 v135, 0
	v_mov_b32_e32 v136, 0
	v_mov_b32_e32 v137, 0
	v_mov_b32_e32 v154, 0
	v_mov_b32_e32 v155, 0
	v_mov_b32_e32 v156, 0
	v_mov_b32_e32 v157, 0
	v_mov_b32_e32 v158, 0
	v_mov_b32_e32 v159, 0
	v_mov_b32_e32 v160, 0
	v_mov_b32_e32 v161, 0
	v_mov_b32_e32 v146, 0
	v_mov_b32_e32 v147, 0
	v_mov_b32_e32 v148, 0
	v_mov_b32_e32 v149, 0
	v_mov_b32_e32 v150, 0
	v_mov_b32_e32 v151, 0
	v_mov_b32_e32 v152, 0
	v_mov_b32_e32 v153, 0
	v_mov_b32_e32 v3, v2
	v_mov_b32_e32 v4, v2
	v_mov_b32_e32 v5, v2
	v_mov_b32_e32 v6, v2
	v_mov_b32_e32 v7, v2
	v_mov_b32_e32 v8, v2
	v_mov_b32_e32 v9, v2
	v_mov_b32_e32 v10, v2
	v_mov_b32_e32 v11, v2
	v_mov_b32_e32 v12, v2
	v_mov_b32_e32 v13, v2
	v_mov_b32_e32 v14, v2
	v_mov_b32_e32 v15, v2
	v_mov_b32_e32 v16, v2
	v_mov_b32_e32 v17, v2
	v_mov_b32_e32 v18, v2
	v_mov_b32_e32 v19, v2
	v_mov_b32_e32 v20, v2
	v_mov_b32_e32 v21, v2
	v_mov_b32_e32 v22, v2
	v_mov_b32_e32 v23, v2
	v_mov_b32_e32 v24, v2
	v_mov_b32_e32 v25, v2
	v_mov_b32_e32 v26, v2
	v_mov_b32_e32 v27, v2
	v_mov_b32_e32 v28, v2
	v_mov_b32_e32 v29, v2
	v_mov_b32_e32 v30, v2
	v_mov_b32_e32 v31, v2
	v_mov_b32_e32 v32, v2
	v_mov_b32_e32 v33, v2
	v_mov_b32_e32 v50, v2
	v_mov_b32_e32 v51, v2
	v_mov_b32_e32 v52, v2
	v_mov_b32_e32 v53, v2
	v_mov_b32_e32 v54, v2
	v_mov_b32_e32 v55, v2
	v_mov_b32_e32 v56, v2
	v_mov_b32_e32 v57, v2
	v_mov_b32_e32 v58, v2
	v_mov_b32_e32 v59, v2
	v_mov_b32_e32 v60, v2
	v_mov_b32_e32 v61, v2
	v_mov_b32_e32 v62, v2
	v_mov_b32_e32 v63, v2
	v_mov_b32_e32 v64, v2
	v_mov_b32_e32 v65, v2
	v_mov_b32_e32 v34, v2
	v_mov_b32_e32 v35, v2
	v_mov_b32_e32 v36, v2
	v_mov_b32_e32 v37, v2
	v_mov_b32_e32 v38, v2
	v_mov_b32_e32 v39, v2
	v_mov_b32_e32 v40, v2
	v_mov_b32_e32 v41, v2
	v_mov_b32_e32 v42, v2
	v_mov_b32_e32 v43, v2
	v_mov_b32_e32 v44, v2
	v_mov_b32_e32 v45, v2
	v_mov_b32_e32 v46, v2
	v_mov_b32_e32 v47, v2
	v_mov_b32_e32 v48, v2
	v_mov_b32_e32 v49, v2
	v_mov_b32_e32 v186, v2
	v_mov_b32_e32 v187, v2
	v_mov_b32_e32 v184, v2
	v_mov_b32_e32 v185, v2
	v_mov_b32_e32 v190, v2
	v_mov_b32_e32 v191, v2
	v_mov_b32_e32 v188, v2
	v_mov_b32_e32 v189, v2

; DI void attn_unit_a8(unsigned char* lds, const AttnArgs& a) {
;     ...
;     auto w_store = [&](int j) __attribute__((always_inline)) { const float* src; unsigned char* dst; int ld, n0, k0; bool gu; w_decode(j, src, dst, ld, n0, k0, gu);
;         const int nb = n0 >> 8; const unsigned uni = (unsigned)(gu ? (nb & 3) * 512 + (nb >> 2) * 128 : nb * 256) * 1024u + (unsigned)k0;
;         const unsigned off = (gu ? wper_gu : wper_dn) + uni;
;         const unsigned* t = (const unsigned*)(lds + AT_WT + wcol * WPITCH + 16 * whalf);
;         *(u32x4*)(dst + off) = (u32x4){t[0], t[1], t[2], t[3]}; };
.Lmy_rd0_noc:
	ds_read2_b32 v[244:245], v253 offset1:1
	ds_read2_b32 v[246:247], v253 offset0:2 offset1:3
	s_cmpk_gt_i32 s42, 0x1ff
	s_cbranch_scc1 .Lmy_rd0_sdum
	s_add_i32 s72, s61, -2
	s_cmp_lt_u32 s72, 24
	s_cbranch_scc0 .Lmy_rd0_sdum
	s_andn2_b32 s73, s65, 1
	s_add_u32 s82, s70, s73
	s_addc_u32 s83, s71, 0
	s_bitcmp1_b32 s65, 0
	s_cbranch_scc1 .Lmy_rd0_sdn
	s_waitcnt lgkmcnt(0)
	global_store_dwordx4 v254, v[244:247], s[82:83]
	s_branch .Lmy_rd0_sdone

; DI void attn_unit_a8(unsigned char* lds, const AttnArgs& a) {
;     ...
;     auto w_store = [&](int j) __attribute__((always_inline)) { const float* src; unsigned char* dst; int ld, n0, k0; bool gu; w_decode(j, src, dst, ld, n0, k0, gu);
;         const int nb = n0 >> 8; const unsigned uni = (unsigned)(gu ? (nb & 3) * 512 + (nb >> 2) * 128 : nb * 256) * 1024u + (unsigned)k0;
;         const unsigned off = (gu ? wper_gu : wper_dn) + uni;
;         const unsigned* t = (const unsigned*)(lds + AT_WT + wcol * WPITCH + 16 * whalf);
;         *(u32x4*)(dst + off) = (u32x4){t[0], t[1], t[2], t[3]}; };
.Lmy_rd0_ldum:
.Lmy_rd0_sdum:
	s_add_u32 s82, s70, 0x1c094000
	s_addc_u32 s83, s71, 0
	s_waitcnt lgkmcnt(0)
	global_store_dwordx4 v254, v[244:247], s[82:83]
.Lmy_rd0_sdone:
	s_cmpk_gt_i32 s42, 0x1ff
	s_cbranch_scc1 .Lmy_rd0_ld0
	s_cmp_lt_u32 s61, 24
	s_cbranch_scc1 .Lmy_rd0_lgo

; DI f32x16 mfma8(v8i a, v8i b, f32x16 c) { return __builtin_amdgcn_mfma_scale_f32_32x32x64_f8f6f4(a, b, c, 0, 0, 0, 0, 0, 0); }
; DI void attn_unit_a8(unsigned char* lds, const AttnArgs& a) {
;     ...
;     auto w_issue = [&](int j) __attribute__((always_inline)) { const float* src; unsigned char* dst; int ld, n0, k0; bool gu; w_decode(j, src, dst, ld, n0, k0, gu);
;         const float* p = src + (size_t)(k0 + 4 * wid) * ld + n0 + wn4;
;         wq[0] = __builtin_nontemporal_load((const f32x4*)p); wq[1] = __builtin_nontemporal_load((const f32x4*)(p + ld));
;         wq[2] = __builtin_nontemporal_load((const f32x4*)(p + (size_t)2 * ld)); wq[3] = __builtin_nontemporal_load((const f32x4*)(p + (size_t)3 * ld)); };
; DI void attn_unit_d8(unsigned char* lds, const AttnArgs& a) {
;     ...
;         lstore(s3, kreg0, vreg0); lstore(s4, kreg1, vreg1);
;         __syncthreads();
;         sb = s2;
;     }
;     o0[0] = mfma8(vY0, PaY, o0[0]); o1[0] = mfma8(vY0, PbY, o1[0]); o0[1] = mfma8(vY1, PaY, o0[1]); o1[1] = mfma8(vY1, PbY, o1[1]);
;     __builtin_amdgcn_s_setprio(0);
;     float lt0 = l0[0] + l0[1] + l0[2] + l0[3]; lt0 += __shfl_xor(lt0, 32);
;     float lt1 = l1[0] + l1[1] + l1[2] + l1[3]; lt1 += __shfl_xor(lt1, 32);
;     unsigned char* op = a.out8 + (size_t)(wid * 32 + r) * 1024 + 4 * h;
;     const float r0 = 16.0f / lt0, r1 = 16.0f * a.lam / lt1;
;     float ss = 0.f;
; #pragma unroll
;     for (int d = 0; d < 2; ++d)
; #pragma unroll
;         for (int i = 0; i < 16; ++i) { const float v = o0[d][i] * r0 - o1[d][i] * r1; o0[d][i] = v; ss += v * v; }
;     ss += __shfl_xor(ss, 32);
;     const float rinv = rsqrtf(ss * (1.0f / 64.0f) + EPS) * a.oscale * CAT_SCALE;
.Lmy_rd0_lgo:
	global_load_dwordx4 v[236:239], v235, s[84:85] nt
	s_add_u32 s84, s84, s80
	s_addc_u32 s85, s85, 0
	global_load_dwordx4 v[240:243], v235, s[84:85] nt
	s_add_u32 s84, s84, s80
	s_addc_u32 s85, s85, 0
	global_load_dwordx4 v[244:247], v235, s[84:85] nt
	s_add_u32 s84, s84, s80
	s_addc_u32 s85, s85, 0
	global_load_dwordx4 v[248:251], v235, s[84:85] nt
	s_mov_b32 s65, s58
	s_mov_b32 s58, s79
	v_xor_b32_e32 v252, 0x4000, v252
	v_xor_b32_e32 v253, 0x4000, v253
	s_add_i32 s61, s61, 1
	s_add_i32 s18, s46, 2
	s_cmpk_lt_u32 s46, 0x42
	s_mov_b32 s46, s18
	s_waitcnt vmcnt(6)
	ds_write_b64 v224, v[192:193]
	v_mfma_f32_32x32x64_f8f6f4 v[66:81], v[98:105], v[122:129], 0
	v_add_u32_e32 v98, 0x1400, v225
	v_add_u32_e32 v99, 0x1400, v107
	ds_write2_b32 v98, v202, v203 offset1:8
	s_waitcnt vmcnt(5)
	ds_write_b64 v106, v[194:195]
	ds_write2_b32 v99, v204, v205 offset1:8
	s_waitcnt lgkmcnt(0)
	s_barrier
	s_cbranch_scc1 .LBB0_663
	s_lshl_b64 s[14:15], s[14:15], 10
	s_add_u32 s6, s8, s14
	s_addc_u32 s15, s9, s15
	s_add_u32 s14, s6, s43
	v_mfma_f32_32x32x64_f8f6f4 v[50:65], v[154:161], v[138:145], v[50:65]
	s_addc_u32 s15, s15, 0
	v_mfma_f32_32x32x64_f8f6f4 v[2:17], v[154:161], v[130:137], v[2:17]
	v_mfma_f32_32x32x64_f8f6f4 v[34:49], v[146:153], v[138:145], v[34:49]
	v_mfma_f32_32x32x64_f8f6f4 v[18:33], v[146:153], v[130:137], v[18:33]
	s_setprio 0
	v_add_f32_e32 v66, v186, v187
	v_add_f32_e32 v66, v184, v66
	v_add_f32_e32 v66, v185, v66
	ds_bpermute_b32 v67, v1, v66
	v_add_f32_e32 v68, v190, v191
	v_add_f32_e32 v68, v188, v68
	v_add_f32_e32 v68, v189, v68
	ds_bpermute_b32 v69, v1, v68
	s_waitcnt lgkmcnt(1)
	v_add_f32_e32 v66, v66, v67
	v_div_scale_f32 v67, s[16:17], v66, v66, s36
	v_rcp_f32_e32 v70, v67
	s_waitcnt lgkmcnt(0)
	v_add_f32_e32 v68, v68, v69
	v_lshlrev_b32_e32 v178, 2, v214
	s_add_i32 s42, s42, s64
	v_fma_f32 v69, -v67, v70, 1.0
	v_fmac_f32_e32 v70, v69, v70
	v_div_scale_f32 v69, vcc, s36, v66, s36
	v_mul_f32_e32 v71, v69, v70
	v_fma_f32 v72, -v67, v71, v69
	v_fmac_f32_e32 v71, v72, v70
	v_fma_f32 v67, -v67, v71, v69
	v_div_scale_f32 v69, s[16:17], v68, v68, v211
	v_rcp_f32_e32 v72, v69
	v_div_fmas_f32 v67, v67, v70, v71
	v_div_fixup_f32 v66, v67, v66, s36
	s_cmpk_gt_i32 s42, 0x21f
	v_fma_f32 v67, -v69, v72, 1.0
	v_fmac_f32_e32 v72, v67, v72
	v_div_scale_f32 v67, vcc, v211, v68, v211
	v_mul_f32_e32 v70, v67, v72
	v_fma_f32 v71, -v69, v70, v67
	v_fmac_f32_e32 v70, v71, v72
	v_fma_f32 v67, -v69, v70, v67
	v_div_fmas_f32 v67, v67, v72, v70
	v_div_fixup_f32 v68, v67, v68, v211
	v_mul_f32_e32 v2, v2, v68
	v_fma_f32 v50, v50, v66, -v2
	v_mul_f32_e32 v2, v3, v68
	v_fma_f32 v51, v51, v66, -v2
	v_mul_f32_e32 v67, v51, v51
	v_mul_f32_e32 v2, v4, v68
	v_fmac_f32_e32 v67, v50, v50
	v_fma_f32 v52, v52, v66, -v2
	v_mul_f32_e32 v2, v5, v68
	v_fmac_f32_e32 v67, v52, v52
	v_fma_f32 v53, v53, v66, -v2
	v_mul_f32_e32 v2, v6, v68
	v_fmac_f32_e32 v67, v53, v53
	v_fma_f32 v54, v54, v66, -v2
	v_mul_f32_e32 v2, v7, v68
	v_fmac_f32_e32 v67, v54, v54
	v_fma_f32 v55, v55, v66, -v2
	v_mul_f32_e32 v2, v8, v68
	v_fmac_f32_e32 v67, v55, v55
	v_fma_f32 v56, v56, v66, -v2
	v_mul_f32_e32 v2, v9, v68
	v_fmac_f32_e32 v67, v56, v56
	v_fma_f32 v57, v57, v66, -v2
	v_mul_f32_e32 v2, v10, v68
	v_fmac_f32_e32 v67, v57, v57
	v_fma_f32 v58, v58, v66, -v2
	v_mul_f32_e32 v2, v11, v68
	v_fmac_f32_e32 v67, v58, v58
	v_fma_f32 v59, v59, v66, -v2
	v_mul_f32_e32 v2, v12, v68
	v_fmac_f32_e32 v67, v59, v59
	v_fma_f32 v60, v60, v66, -v2
	v_mul_f32_e32 v2, v13, v68
	v_fmac_f32_e32 v67, v60, v60
	v_fma_f32 v61, v61, v66, -v2
	v_mul_f32_e32 v14, v14, v68
	v_fmac_f32_e32 v67, v61, v61
	v_fma_f32 v62, v62, v66, -v14
	v_mul_f32_e32 v14, v15, v68
	v_fmac_f32_e32 v67, v62, v62
	v_fma_f32 v63, v63, v66, -v14
	v_mul_f32_e32 v14, v16, v68
	v_lshlrev_b32_e32 v69, 4, v214
	v_fmac_f32_e32 v67, v63, v63
	v_fma_f32 v64, v64, v66, -v14
	v_mul_f32_e32 v14, v17, v68
	global_load_dwordx4 v[2:5], v69, s[10:11] offset:224
	global_load_dwordx4 v[6:9], v69, s[10:11] offset:32
	global_load_dwordx4 v[10:13], v69, s[10:11]
	v_fmac_f32_e32 v67, v64, v64
	v_fma_f32 v65, v65, v66, -v14
	v_mul_f32_e32 v14, v18, v68
	v_fmac_f32_e32 v67, v65, v65
	v_fma_f32 v70, v34, v66, -v14
	v_mul_f32_e32 v14, v19, v68
	v_fmac_f32_e32 v67, v70, v70
	v_fma_f32 v71, v35, v66, -v14
	v_mul_f32_e32 v14, v20, v68
	v_fmac_f32_e32 v67, v71, v71
	v_fma_f32 v72, v36, v66, -v14
	v_mul_f32_e32 v14, v21, v68
	v_fmac_f32_e32 v67, v72, v72
	v_fma_f32 v73, v37, v66, -v14
	v_mul_f32_e32 v14, v22, v68
	v_fmac_f32_e32 v67, v73, v73
	v_fma_f32 v74, v38, v66, -v14
	v_mul_f32_e32 v14, v23, v68
	v_fmac_f32_e32 v67, v74, v74
	v_fma_f32 v75, v39, v66, -v14
	v_fmac_f32_e32 v67, v75, v75
	v_pk_mul_f32 v[14:15], v[24:25], v[68:69] op_sel_hi:[1,0]
	v_pk_mul_f32 v[22:23], v[32:33], v[68:69] op_sel_hi:[1,0]
	v_pk_fma_f32 v[34:35], v[40:41], v[66:67], v[14:15] op_sel_hi:[1,0,1] neg_lo:[0,0,1] neg_hi:[0,0,1]
	s_nop 0
	v_pk_mul_f32 v[14:15], v[34:35], v[34:35]
	s_nop 0
	v_add_f32_e32 v14, v14, v67
	v_add_f32_e32 v20, v15, v14
	v_pk_mul_f32 v[14:15], v[26:27], v[68:69] op_sel_hi:[1,0]
	s_nop 0
	v_pk_fma_f32 v[36:37], v[42:43], v[66:67], v[14:15] op_sel_hi:[1,0,1] neg_lo:[0,0,1] neg_hi:[0,0,1]
	global_load_dwordx4 v[14:17], v69, s[10:11] offset:64
	v_pk_mul_f32 v[18:19], v[36:37], v[36:37]
	v_pk_fma_f32 v[42:43], v[48:49], v[66:67], v[22:23] op_sel_hi:[1,0,1] neg_lo:[0,0,1] neg_hi:[0,0,1]
	v_add_f32_e32 v18, v18, v20
	v_add_f32_e32 v20, v19, v18
	v_pk_mul_f32 v[18:19], v[28:29], v[68:69] op_sel_hi:[1,0]
	v_pk_mul_f32 v[22:23], v[42:43], v[42:43]
	v_pk_fma_f32 v[38:39], v[44:45], v[66:67], v[18:19] op_sel_hi:[1,0,1] neg_lo:[0,0,1] neg_hi:[0,0,1]
	s_nop 0
	v_pk_mul_f32 v[18:19], v[38:39], v[38:39]
	s_nop 0
	v_add_f32_e32 v18, v18, v20
	v_add_f32_e32 v20, v19, v18
	v_pk_mul_f32 v[18:19], v[30:31], v[68:69] op_sel_hi:[1,0]
	s_nop 0
	v_pk_fma_f32 v[40:41], v[46:47], v[66:67], v[18:19] op_sel_hi:[1,0,1] neg_lo:[0,0,1] neg_hi:[0,0,1]
	s_nop 0
	v_pk_mul_f32 v[18:19], v[40:41], v[40:41]
	s_nop 0
	v_add_f32_e32 v18, v18, v20
	v_add_f32_e32 v24, v19, v18
	v_add_f32_e32 v22, v22, v24
	v_add_f32_e32 v26, v23, v22
	ds_bpermute_b32 v27, v1, v26
	global_load_dwordx4 v[18:21], v69, s[10:11] offset:96
	global_load_dwordx4 v[22:25], v69, s[10:11] offset:192
	s_waitcnt lgkmcnt(0)
; DI unsigned pk4_fp8(float a, float b, float c, float d) { int r = 0; r = __builtin_amdgcn_cvt_pk_fp8_f32(a, b, r, false); r = __builtin_amdgcn_cvt_pk_fp8_f32(c, d, r, true); return (unsigned)r; }
; DI float clamp448(float x) { return __builtin_amdgcn_fmed3f(x, -448.0f, 448.0f); }
; DI void attn_unit_d8(unsigned char* lds, const AttnArgs& a) {
;     ...
;     const float r0 = 16.0f / lt0, r1 = 16.0f * a.lam / lt1;
;     float ss = 0.f;
; #pragma unroll
;     for (int d = 0; d < 2; ++d)
; #pragma unroll
;         for (int i = 0; i < 16; ++i) { const float v = o0[d][i] * r0 - o1[d][i] * r1; o0[d][i] = v; ss += v * v; }
;     ss += __shfl_xor(ss, 32);
;     const float rinv = rsqrtf(ss * (1.0f / 64.0f) + EPS) * a.oscale * CAT_SCALE;
;     f32x4 ggv[2][4];
; #pragma unroll
;     for (int d = 0; d < 2; ++d)
; #pragma unroll
;         for (int g = 0; g < 4; ++g) ggv[d][g] = *(const f32x4*)(a.subg + 32 * d + 8 * g + 4 * h);
;     asm volatile("" : "+v"(ggv[0][0]), "+v"(ggv[1][3]));
; #pragma unroll
;     for (int d = 0; d < 2; ++d)
; #pragma unroll
;         for (int g = 0; g < 4; ++g) { const f32x4 gg = ggv[d][g];
;             *(unsigned*)(op + 32 * d + 8 * g) = pk4_fp8(clamp448(o0[d][4 * g] * rinv * gg[0]), clamp448(o0[d][4 * g + 1] * rinv * gg[1]), clamp448(o0[d][4 * g + 2] * rinv * gg[2]), clamp448(o0[d][4 * g + 3] * rinv * gg[3])); }
	v_add_f32_e32 v26, v26, v27
	v_fmamk_f32 v26, v26, 0x3c800000, v212
	v_mul_f32_e32 v27, 0x4b800000, v26
	v_cmp_gt_f32_e32 vcc, s39, v26
	s_nop 1
	v_cndmask_b32_e32 v30, v26, v27, vcc
	global_load_dwordx4 v[26:29], v69, s[10:11] offset:128
	v_rsq_f32_e32 v32, v30
	v_lshlrev_b64 v[30:31], 10, v[180:181]
	v_lshl_add_u64 v[44:45], s[14:15], 0, v[30:31]
	v_lshl_add_u64 v[44:45], v[44:45], 0, v[178:179]
	v_mul_f32_e32 v30, 0x45800000, v32
	v_cndmask_b32_e32 v30, v32, v30, vcc
	v_mul_f32_e32 v48, 0x3f4ccccd, v30
	global_load_dwordx4 v[30:33], v69, s[10:11] offset:160
	v_mul_f32_e32 v48, 0x41800000, v48
	s_waitcnt vmcnt(5)
	v_mul_f32_e32 v49, v50, v48
	v_mul_f32_e32 v10, v10, v49
	v_mul_f32_e32 v49, v51, v48
	v_mul_f32_e32 v11, v11, v49
	v_mul_f32_e32 v49, v52, v48
	v_med3_f32 v10, v10, s40, v213
	v_med3_f32 v11, v11, s40, v213
	v_mul_f32_e32 v12, v12, v49
	s_nop 0
	v_cvt_pk_fp8_f32 v49, v10, v11
	v_mul_f32_e32 v10, v53, v48
	v_mul_f32_e32 v10, v13, v10
	v_med3_f32 v12, v12, s40, v213
	v_med3_f32 v10, v10, s40, v213
	v_cvt_pk_fp8_f32 v49, v12, v10 op_sel:[0,0,1]
	v_mul_f32_e32 v10, v54, v48
	v_mul_f32_e32 v6, v6, v10
	v_mul_f32_e32 v10, v55, v48
	v_mul_f32_e32 v7, v7, v10
	v_mul_f32_e32 v10, v56, v48
	v_med3_f32 v6, v6, s40, v213
	v_med3_f32 v7, v7, s40, v213
	v_mul_f32_e32 v8, v8, v10
	s_nop 0
	v_cvt_pk_fp8_f32 v10, v6, v7
	v_mul_f32_e32 v6, v57, v48
	v_mul_f32_e32 v6, v9, v6
	v_med3_f32 v8, v8, s40, v213
	v_med3_f32 v6, v6, s40, v213
	v_cvt_pk_fp8_f32 v10, v8, v6 op_sel:[0,0,1]
	v_add_co_u32_e32 v6, vcc, s41, v44
	v_lshl_add_u64 v[46:47], v[44:45], 0, s[12:13]
	s_nop 0
	v_addc_co_u32_e32 v7, vcc, 0, v45, vcc
	global_store_dword v[6:7], v49, off offset:768
	global_store_dword v[46:47], v10, off offset:8
	v_mul_f32_e32 v6, v58, v48
	v_mul_f32_e32 v7, v59, v48
	s_waitcnt vmcnt(6)
	v_mul_f32_e32 v6, v14, v6
	v_mul_f32_e32 v7, v15, v7
	v_med3_f32 v6, v6, s40, v213
	v_med3_f32 v7, v7, s40, v213
	s_nop 0
	v_cvt_pk_fp8_f32 v9, v6, v7
	v_mul_f32_e32 v8, v60, v48
	v_mul_f32_e32 v6, v61, v48
	v_mul_f32_e32 v8, v16, v8
	v_mul_f32_e32 v6, v17, v6
	v_med3_f32 v8, v8, s40, v213
	v_med3_f32 v6, v6, s40, v213
	v_cvt_pk_fp8_f32 v9, v8, v6 op_sel:[0,0,1]
	v_mul_f32_e32 v6, v62, v48
	v_mul_f32_e32 v7, v63, v48
	s_nop 0
	v_mul_f32_e32 v8, v64, v48
	s_nop 0
	s_waitcnt vmcnt(5)
	v_mul_f32_e32 v6, v18, v6
	v_mul_f32_e32 v7, v19, v7
	v_med3_f32 v6, v6, s40, v213
	v_med3_f32 v7, v7, s40, v213
	v_cvt_pk_fp8_f32 v10, v6, v7
	v_mul_f32_e32 v6, v65, v48
	v_mul_f32_e32 v8, v20, v8
	v_mul_f32_e32 v6, v21, v6
	v_med3_f32 v8, v8, s40, v213
	v_med3_f32 v6, v6, s40, v213
	v_cvt_pk_fp8_f32 v10, v8, v6 op_sel:[0,0,1]
	v_mul_f32_e32 v6, v70, v48
	v_mul_f32_e32 v7, v71, v48
	s_waitcnt vmcnt(3)
	v_mul_f32_e32 v6, v26, v6
	v_mul_f32_e32 v7, v27, v7
	v_med3_f32 v6, v6, s40, v213
	v_med3_f32 v7, v7, s40, v213
	v_cvt_pk_fp8_f32 v11, v6, v7
	v_mul_f32_e32 v8, v72, v48
	v_mul_f32_e32 v6, v73, v48
	v_mul_f32_e32 v8, v28, v8
	v_mul_f32_e32 v6, v29, v6
	v_med3_f32 v8, v8, s40, v213
	v_med3_f32 v6, v6, s40, v213
	v_cvt_pk_fp8_f32 v11, v8, v6 op_sel:[0,0,1]
	v_mul_f32_e32 v6, v74, v48
	v_mul_f32_e32 v7, v75, v48
	s_waitcnt vmcnt(2)
	v_mul_f32_e32 v6, v30, v6
	v_mul_f32_e32 v7, v31, v7
	v_med3_f32 v6, v6, s40, v213
	v_med3_f32 v7, v7, s40, v213
	s_nop 0
	v_cvt_pk_fp8_f32 v12, v6, v7
	v_mul_f32_e32 v8, v34, v48
	v_mul_f32_e32 v6, v35, v48
	v_mul_f32_e32 v8, v32, v8
	v_mul_f32_e32 v6, v33, v6
	v_med3_f32 v8, v8, s40, v213
	v_med3_f32 v6, v6, s40, v213
	v_cvt_pk_fp8_f32 v12, v8, v6 op_sel:[0,0,1]
	v_mul_f32_e32 v6, v36, v48
	v_mul_f32_e32 v7, v37, v48
	v_mul_f32_e32 v6, v22, v6
	v_mul_f32_e32 v7, v23, v7
	global_store_dword v[46:47], v9, off offset:16
	global_store_dword v[46:47], v10, off offset:24
	global_store_dword v[46:47], v11, off offset:32
	global_store_dword v[46:47], v12, off offset:40
	v_med3_f32 v6, v6, s40, v213
	v_med3_f32 v7, v7, s40, v213
	s_nop 0
	v_cvt_pk_fp8_f32 v9, v6, v7
	v_mul_f32_e32 v8, v38, v48
	v_mul_f32_e32 v6, v39, v48
	v_mul_f32_e32 v8, v24, v8
	v_mul_f32_e32 v6, v25, v6
	v_med3_f32 v8, v8, s40, v213
	v_med3_f32 v6, v6, s40, v213
	v_cvt_pk_fp8_f32 v9, v8, v6 op_sel:[0,0,1]
	v_mul_f32_e32 v6, v40, v48
	v_mul_f32_e32 v2, v2, v6
	v_mul_f32_e32 v6, v41, v48
	v_mul_f32_e32 v3, v3, v6
	v_mul_f32_e32 v6, v42, v48
	v_med3_f32 v2, v2, s40, v213
	v_med3_f32 v3, v3, s40, v213
	v_mul_f32_e32 v4, v4, v6
	s_nop 0
	v_cvt_pk_fp8_f32 v6, v2, v3
	v_mul_f32_e32 v2, v43, v48
	v_mul_f32_e32 v2, v5, v2
	v_med3_f32 v4, v4, s40, v213
	v_med3_f32 v2, v2, s40, v213
	v_cvt_pk_fp8_f32 v6, v4, v2 op_sel:[0,0,1]
	global_store_dword v[46:47], v9, off offset:48
	global_store_dword v[46:47], v6, off offset:56
	s_cbranch_scc0 .LBB0_656

; DI void attn_unit_d8(unsigned char* lds, const AttnArgs& a) {
;     ...
;     f32x16 o0[2], o1[2];
; #pragma unroll
;     for (int d = 0; d < 2; ++d) { o0[d] = (f32x16){}; o1[d] = (f32x16){}; }
;     f32x4 l0 = {0.f, 0.f, 0.f, 0.f}, l1 = {0.f, 0.f, 0.f, 0.f};
;     ...
;     if (wid >= 4) __builtin_amdgcn_s_setprio(1);
;     int sb = 0;
;     const v8i zz8 = (v8i){0, 0, 0, 0, 0, 0, 0, 0};
;     v8i PaX = zz8, PbX = zz8, PaY = zz8, PbY = zz8, vX0 = zz8, vX1 = zz8, vY0 = zz8, vY1 = zz8;
.LBB0_1887:
	s_and_b32 s61, s46, 1
	s_lshl_b32 s61, s61, 3
	s_sub_i32 s61, 0, s61
	s_ashr_i32 s21, s20, 31
	s_lshl_b64 s[20:21], s[20:21], 8
	s_add_u32 s8, s24, s20
	s_addc_u32 s20, s25, s21
	s_add_u32 s8, s8, s47
	s_addc_u32 s21, s20, 0
	s_add_u32 s20, s8, 0x800000
	v_mov_b32_e32 v2, 0
	s_addc_u32 s21, s21, 0
	s_mov_b32 s23, 0
	s_mov_b32 s22, -2
	v_mov_b32_e32 v138, 0
	v_mov_b32_e32 v139, 0
	v_mov_b32_e32 v140, 0
	v_mov_b32_e32 v141, 0
	v_mov_b32_e32 v142, 0
	v_mov_b32_e32 v143, 0
	v_mov_b32_e32 v144, 0
	v_mov_b32_e32 v145, 0
	v_mov_b32_e32 v130, 0
	v_mov_b32_e32 v131, 0
	v_mov_b32_e32 v132, 0
	v_mov_b32_e32 v133, 0
	v_mov_b32_e32 v134, 0
	v_mov_b32_e32 v135, 0
	v_mov_b32_e32 v136, 0
	v_mov_b32_e32 v137, 0
	v_mov_b32_e32 v154, 0
	v_mov_b32_e32 v155, 0
	v_mov_b32_e32 v156, 0
	v_mov_b32_e32 v157, 0
	v_mov_b32_e32 v158, 0
	v_mov_b32_e32 v159, 0
	v_mov_b32_e32 v160, 0
	v_mov_b32_e32 v161, 0
	v_mov_b32_e32 v146, 0
	v_mov_b32_e32 v147, 0
	v_mov_b32_e32 v148, 0
	v_mov_b32_e32 v149, 0
	v_mov_b32_e32 v150, 0
	v_mov_b32_e32 v151, 0
	v_mov_b32_e32 v152, 0
	v_mov_b32_e32 v153, 0
	v_mov_b32_e32 v3, v2
	v_mov_b32_e32 v4, v2
	v_mov_b32_e32 v5, v2
	v_mov_b32_e32 v6, v2
	v_mov_b32_e32 v7, v2
	v_mov_b32_e32 v8, v2
	v_mov_b32_e32 v9, v2
	v_mov_b32_e32 v10, v2
	v_mov_b32_e32 v11, v2
	v_mov_b32_e32 v12, v2
	v_mov_b32_e32 v13, v2
	v_mov_b32_e32 v14, v2
	v_mov_b32_e32 v15, v2
	v_mov_b32_e32 v16, v2
	v_mov_b32_e32 v17, v2
	v_mov_b32_e32 v18, v2
	v_mov_b32_e32 v19, v2
	v_mov_b32_e32 v20, v2
	v_mov_b32_e32 v21, v2
	v_mov_b32_e32 v22, v2
	v_mov_b32_e32 v23, v2
	v_mov_b32_e32 v24, v2
	v_mov_b32_e32 v25, v2
	v_mov_b32_e32 v26, v2
	v_mov_b32_e32 v27, v2
	v_mov_b32_e32 v28, v2
	v_mov_b32_e32 v29, v2
	v_mov_b32_e32 v30, v2
	v_mov_b32_e32 v31, v2
	v_mov_b32_e32 v32, v2
	v_mov_b32_e32 v33, v2
	v_mov_b32_e32 v50, v2
	v_mov_b32_e32 v51, v2
	v_mov_b32_e32 v52, v2
	v_mov_b32_e32 v53, v2
	v_mov_b32_e32 v54, v2
	v_mov_b32_e32 v55, v2
	v_mov_b32_e32 v56, v2
	v_mov_b32_e32 v57, v2
	v_mov_b32_e32 v58, v2
	v_mov_b32_e32 v59, v2
	v_mov_b32_e32 v60, v2
	v_mov_b32_e32 v61, v2
	v_mov_b32_e32 v62, v2
	v_mov_b32_e32 v63, v2
	v_mov_b32_e32 v64, v2
	v_mov_b32_e32 v65, v2
	v_mov_b32_e32 v34, v2
	v_mov_b32_e32 v35, v2
	v_mov_b32_e32 v36, v2
	v_mov_b32_e32 v37, v2
	v_mov_b32_e32 v38, v2
	v_mov_b32_e32 v39, v2
	v_mov_b32_e32 v40, v2
	v_mov_b32_e32 v41, v2
	v_mov_b32_e32 v42, v2
	v_mov_b32_e32 v43, v2
	v_mov_b32_e32 v44, v2
	v_mov_b32_e32 v45, v2
	v_mov_b32_e32 v46, v2
	v_mov_b32_e32 v47, v2
	v_mov_b32_e32 v48, v2
	v_mov_b32_e32 v49, v2
	v_mov_b32_e32 v188, v2
	v_mov_b32_e32 v189, v2
	v_mov_b32_e32 v186, v2
	v_mov_b32_e32 v187, v2
	v_mov_b32_e32 v192, v2
	v_mov_b32_e32 v193, v2
	v_mov_b32_e32 v190, v2
	v_mov_b32_e32 v191, v2

; DI void attn_unit_a8(unsigned char* lds, const AttnArgs& a) {
;     ...
;     auto w_store = [&](int j) __attribute__((always_inline)) { const float* src; unsigned char* dst; int ld, n0, k0; bool gu; w_decode(j, src, dst, ld, n0, k0, gu);
;         const int nb = n0 >> 8; const unsigned uni = (unsigned)(gu ? (nb & 3) * 512 + (nb >> 2) * 128 : nb * 256) * 1024u + (unsigned)k0;
;         const unsigned off = (gu ? wper_gu : wper_dn) + uni;
;         const unsigned* t = (const unsigned*)(lds + AT_WT + wcol * WPITCH + 16 * whalf);
;         *(u32x4*)(dst + off) = (u32x4){t[0], t[1], t[2], t[3]}; };
.Lmy_rd1_noc:
	ds_read2_b32 v[244:245], v253 offset1:1
	ds_read2_b32 v[246:247], v253 offset0:2 offset1:3
	s_cmpk_gt_i32 s46, 0x1ff
	s_cbranch_scc1 .Lmy_rd1_sdum
	s_add_i32 s72, s61, -2
	s_cmp_lt_u32 s72, 24
	s_cbranch_scc0 .Lmy_rd1_sdum
	s_andn2_b32 s73, s65, 1
	s_add_u32 s82, s70, s73
	s_addc_u32 s83, s71, 0
	s_bitcmp1_b32 s65, 0
	s_cbranch_scc1 .Lmy_rd1_sdn
	s_waitcnt lgkmcnt(0)
	global_store_dwordx4 v254, v[244:247], s[82:83]
	s_branch .Lmy_rd1_sdone

; DI void attn_unit_a8(unsigned char* lds, const AttnArgs& a) {
;     ...
;     auto w_issue = [&](int j) __attribute__((always_inline)) { const float* src; unsigned char* dst; int ld, n0, k0; bool gu; w_decode(j, src, dst, ld, n0, k0, gu);
;         const float* p = src + (size_t)(k0 + 4 * wid) * ld + n0 + wn4;
;         wq[0] = __builtin_nontemporal_load((const f32x4*)p); wq[1] = __builtin_nontemporal_load((const f32x4*)(p + ld));
;         wq[2] = __builtin_nontemporal_load((const f32x4*)(p + (size_t)2 * ld)); wq[3] = __builtin_nontemporal_load((const f32x4*)(p + (size_t)3 * ld)); };
.Lmy_rd1_sdone:
	s_cmpk_gt_i32 s46, 0x1ff
	s_cbranch_scc1 .Lmy_rd1_ld0
	s_cmp_lt_u32 s61, 24
	s_cbranch_scc1 .Lmy_rd1_lgo

; DI f32x16 mfma8(v8i a, v8i b, f32x16 c) { return __builtin_amdgcn_mfma_scale_f32_32x32x64_f8f6f4(a, b, c, 0, 0, 0, 0, 0, 0); }
; DI void attn_unit_a8(unsigned char* lds, const AttnArgs& a) {
;     ...
;     auto w_issue = [&](int j) __attribute__((always_inline)) { const float* src; unsigned char* dst; int ld, n0, k0; bool gu; w_decode(j, src, dst, ld, n0, k0, gu);
;         const float* p = src + (size_t)(k0 + 4 * wid) * ld + n0 + wn4;
;         wq[0] = __builtin_nontemporal_load((const f32x4*)p); wq[1] = __builtin_nontemporal_load((const f32x4*)(p + ld));
;         wq[2] = __builtin_nontemporal_load((const f32x4*)(p + (size_t)2 * ld)); wq[3] = __builtin_nontemporal_load((const f32x4*)(p + (size_t)3 * ld)); };
; DI void attn_unit_d8(unsigned char* lds, const AttnArgs& a) {
;     ...
;         lstore(s3, kreg0, vreg0); lstore(s4, kreg1, vreg1);
;         __syncthreads();
;         sb = s2;
;     }
;     o0[0] = mfma8(vY0, PaY, o0[0]); o1[0] = mfma8(vY0, PbY, o1[0]); o0[1] = mfma8(vY1, PaY, o0[1]); o1[1] = mfma8(vY1, PbY, o1[1]);
;     __builtin_amdgcn_s_setprio(0);
;     float lt0 = l0[0] + l0[1] + l0[2] + l0[3]; lt0 += __shfl_xor(lt0, 32);
;     float lt1 = l1[0] + l1[1] + l1[2] + l1[3]; lt1 += __shfl_xor(lt1, 32);
;     unsigned char* op = a.out8 + (size_t)(wid * 32 + r) * 1024 + 4 * h;
;     const float r0 = 16.0f / lt0, r1 = 16.0f * a.lam / lt1;
;     float ss = 0.f;
; #pragma unroll
;     for (int d = 0; d < 2; ++d)
; #pragma unroll
;         for (int i = 0; i < 16; ++i) { const float v = o0[d][i] * r0 - o1[d][i] * r1; o0[d][i] = v; ss += v * v; }
;     ss += __shfl_xor(ss, 32);
;     const float rinv = rsqrtf(ss * (1.0f / 64.0f) + EPS) * a.oscale * CAT_SCALE;
.Lmy_rd1_lgo:
	global_load_dwordx4 v[236:239], v235, s[84:85] nt
	s_add_u32 s84, s84, s80
	s_addc_u32 s85, s85, 0
	global_load_dwordx4 v[240:243], v235, s[84:85] nt
	s_add_u32 s84, s84, s80
	s_addc_u32 s85, s85, 0
	global_load_dwordx4 v[244:247], v235, s[84:85] nt
	s_add_u32 s84, s84, s80
	s_addc_u32 s85, s85, 0
	global_load_dwordx4 v[248:251], v235, s[84:85] nt
	s_mov_b32 s65, s64
	s_mov_b32 s64, s79
	v_xor_b32_e32 v252, 0x4000, v252
	v_xor_b32_e32 v253, 0x4000, v253
	s_add_i32 s61, s61, 1
	s_cmpk_lt_u32 s22, 0x42
	s_waitcnt vmcnt(6)
	ds_write_b64 v224, v[194:195]
	v_mfma_f32_32x32x64_f8f6f4 v[66:81], v[98:105], v[122:129], 0
	v_add_u32_e32 v98, s51, v218
	v_add_u32_e32 v99, 0x1400, v106
	v_add_u32_e32 v98, 0x1400, v98
	ds_write2_b32 v99, v204, v205 offset1:8
	s_waitcnt vmcnt(5)
	ds_write_b64 v107, v[196:197]
	ds_write2_b32 v98, v206, v207 offset1:8
	s_waitcnt lgkmcnt(0)
	s_barrier
	s_cbranch_scc1 .LBB0_1888
	s_lshl_b64 s[16:17], s[16:17], 10
	s_add_u32 s8, s10, s16
	s_addc_u32 s17, s11, s17
	s_add_u32 s16, s8, s47
	v_mfma_f32_32x32x64_f8f6f4 v[50:65], v[154:161], v[138:145], v[50:65]
	s_addc_u32 s17, s17, 0
	v_mfma_f32_32x32x64_f8f6f4 v[2:17], v[154:161], v[130:137], v[2:17]
	v_mfma_f32_32x32x64_f8f6f4 v[34:49], v[146:153], v[138:145], v[34:49]
	v_mfma_f32_32x32x64_f8f6f4 v[18:33], v[146:153], v[130:137], v[18:33]
	s_setprio 0
	v_add_f32_e32 v66, v188, v189
	v_add_f32_e32 v66, v186, v66
	v_add_f32_e32 v66, v187, v66
	ds_bpermute_b32 v67, v1, v66
	v_add_f32_e32 v68, v192, v193
	v_add_f32_e32 v68, v190, v68
	v_add_f32_e32 v68, v191, v68
	ds_bpermute_b32 v69, v1, v68
	s_waitcnt lgkmcnt(1)
	v_add_f32_e32 v66, v66, v67
	v_div_scale_f32 v67, s[18:19], v66, v66, s36
	v_rcp_f32_e32 v70, v67
	s_waitcnt lgkmcnt(0)
	v_add_f32_e32 v68, v68, v69
	v_lshlrev_b32_e32 v178, 2, v217
	s_add_i32 s46, s46, s60
	v_fma_f32 v69, -v67, v70, 1.0
	v_fmac_f32_e32 v70, v69, v70
	v_div_scale_f32 v69, vcc, s36, v66, s36
	v_mul_f32_e32 v71, v69, v70
	v_fma_f32 v72, -v67, v71, v69
	v_fmac_f32_e32 v71, v72, v70
	v_fma_f32 v67, -v67, v71, v69
	v_div_scale_f32 v69, s[18:19], v68, v68, v214
	v_rcp_f32_e32 v72, v69
	v_div_fmas_f32 v67, v67, v70, v71
	v_div_fixup_f32 v66, v67, v66, s36
	s_cmpk_gt_i32 s46, 0x1ff
	v_fma_f32 v67, -v69, v72, 1.0
	v_fmac_f32_e32 v72, v67, v72
	v_div_scale_f32 v67, vcc, v214, v68, v214
	v_mul_f32_e32 v70, v67, v72
	v_fma_f32 v71, -v69, v70, v67
	v_fmac_f32_e32 v70, v71, v72
	v_fma_f32 v67, -v69, v70, v67
	v_div_fmas_f32 v67, v67, v72, v70
	v_div_fixup_f32 v68, v67, v68, v214
	v_mul_f32_e32 v2, v2, v68
	v_fma_f32 v50, v50, v66, -v2
	v_mul_f32_e32 v2, v3, v68
	v_fma_f32 v51, v51, v66, -v2
	v_mul_f32_e32 v67, v51, v51
	v_mul_f32_e32 v2, v4, v68
	v_fmac_f32_e32 v67, v50, v50
	v_fma_f32 v52, v52, v66, -v2
	v_mul_f32_e32 v2, v5, v68
	v_fmac_f32_e32 v67, v52, v52
	v_fma_f32 v53, v53, v66, -v2
	v_mul_f32_e32 v2, v6, v68
	v_fmac_f32_e32 v67, v53, v53
	v_fma_f32 v54, v54, v66, -v2
	v_mul_f32_e32 v2, v7, v68
	v_fmac_f32_e32 v67, v54, v54
	v_fma_f32 v55, v55, v66, -v2
	v_mul_f32_e32 v2, v8, v68
	v_fmac_f32_e32 v67, v55, v55
	v_fma_f32 v56, v56, v66, -v2
	v_mul_f32_e32 v2, v9, v68
	v_fmac_f32_e32 v67, v56, v56
	v_fma_f32 v57, v57, v66, -v2
	v_mul_f32_e32 v2, v10, v68
	v_fmac_f32_e32 v67, v57, v57
	v_fma_f32 v58, v58, v66, -v2
	v_mul_f32_e32 v2, v11, v68
	v_fmac_f32_e32 v67, v58, v58
	v_fma_f32 v59, v59, v66, -v2
	v_mul_f32_e32 v2, v12, v68
	v_fmac_f32_e32 v67, v59, v59
	v_fma_f32 v60, v60, v66, -v2
	v_mul_f32_e32 v2, v13, v68
	v_fmac_f32_e32 v67, v60, v60
	v_fma_f32 v61, v61, v66, -v2
	v_mul_f32_e32 v14, v14, v68
	v_fmac_f32_e32 v67, v61, v61
	v_fma_f32 v62, v62, v66, -v14
	v_mul_f32_e32 v14, v15, v68
	v_fmac_f32_e32 v67, v62, v62
	v_fma_f32 v63, v63, v66, -v14
	v_mul_f32_e32 v14, v16, v68
	v_lshlrev_b32_e32 v69, 4, v217
	v_fmac_f32_e32 v67, v63, v63
	v_fma_f32 v64, v64, v66, -v14
	v_mul_f32_e32 v14, v17, v68
	global_load_dwordx4 v[2:5], v69, s[12:13] offset:480
	global_load_dwordx4 v[6:9], v69, s[12:13] offset:288
	global_load_dwordx4 v[10:13], v69, s[12:13] offset:256
	v_fmac_f32_e32 v67, v64, v64
	v_fma_f32 v65, v65, v66, -v14
	v_mul_f32_e32 v14, v18, v68
	v_fmac_f32_e32 v67, v65, v65
	v_fma_f32 v70, v34, v66, -v14
	v_mul_f32_e32 v14, v19, v68
	v_fmac_f32_e32 v67, v70, v70
	v_fma_f32 v71, v35, v66, -v14
	v_mul_f32_e32 v14, v20, v68
	v_fmac_f32_e32 v67, v71, v71
	v_fma_f32 v72, v36, v66, -v14
	v_mul_f32_e32 v14, v21, v68
	v_fmac_f32_e32 v67, v72, v72
	v_fma_f32 v73, v37, v66, -v14
	v_mul_f32_e32 v14, v22, v68
	v_fmac_f32_e32 v67, v73, v73
	v_fma_f32 v74, v38, v66, -v14
	v_mul_f32_e32 v14, v23, v68
	v_fmac_f32_e32 v67, v74, v74
	v_fma_f32 v75, v39, v66, -v14
	v_fmac_f32_e32 v67, v75, v75
	v_pk_mul_f32 v[14:15], v[24:25], v[68:69] op_sel_hi:[1,0]
	v_pk_mul_f32 v[22:23], v[32:33], v[68:69] op_sel_hi:[1,0]
	v_pk_fma_f32 v[34:35], v[40:41], v[66:67], v[14:15] op_sel_hi:[1,0,1] neg_lo:[0,0,1] neg_hi:[0,0,1]
	s_nop 0
	v_pk_mul_f32 v[14:15], v[34:35], v[34:35]
	s_nop 0
	v_add_f32_e32 v14, v14, v67
	v_add_f32_e32 v20, v15, v14
	v_pk_mul_f32 v[14:15], v[26:27], v[68:69] op_sel_hi:[1,0]
	s_nop 0
	v_pk_fma_f32 v[36:37], v[42:43], v[66:67], v[14:15] op_sel_hi:[1,0,1] neg_lo:[0,0,1] neg_hi:[0,0,1]
	global_load_dwordx4 v[14:17], v69, s[12:13] offset:320
	v_pk_mul_f32 v[18:19], v[36:37], v[36:37]
	v_pk_fma_f32 v[42:43], v[48:49], v[66:67], v[22:23] op_sel_hi:[1,0,1] neg_lo:[0,0,1] neg_hi:[0,0,1]
	v_add_f32_e32 v18, v18, v20
	v_add_f32_e32 v20, v19, v18
	v_pk_mul_f32 v[18:19], v[28:29], v[68:69] op_sel_hi:[1,0]
	v_pk_mul_f32 v[22:23], v[42:43], v[42:43]
	v_pk_fma_f32 v[38:39], v[44:45], v[66:67], v[18:19] op_sel_hi:[1,0,1] neg_lo:[0,0,1] neg_hi:[0,0,1]
	s_nop 0
	v_pk_mul_f32 v[18:19], v[38:39], v[38:39]
	s_nop 0
	v_add_f32_e32 v18, v18, v20
	v_add_f32_e32 v20, v19, v18
	v_pk_mul_f32 v[18:19], v[30:31], v[68:69] op_sel_hi:[1,0]
	s_nop 0
	v_pk_fma_f32 v[40:41], v[46:47], v[66:67], v[18:19] op_sel_hi:[1,0,1] neg_lo:[0,0,1] neg_hi:[0,0,1]
	s_nop 0
	v_pk_mul_f32 v[18:19], v[40:41], v[40:41]
	s_nop 0
	v_add_f32_e32 v18, v18, v20
	v_add_f32_e32 v24, v19, v18
	v_add_f32_e32 v22, v22, v24
	v_add_f32_e32 v26, v23, v22
	ds_bpermute_b32 v27, v1, v26
	global_load_dwordx4 v[18:21], v69, s[12:13] offset:352
	global_load_dwordx4 v[22:25], v69, s[12:13] offset:448
	s_waitcnt lgkmcnt(0)
; DI unsigned pk4_fp8(float a, float b, float c, float d) { int r = 0; r = __builtin_amdgcn_cvt_pk_fp8_f32(a, b, r, false); r = __builtin_amdgcn_cvt_pk_fp8_f32(c, d, r, true); return (unsigned)r; }
; DI float clamp448(float x) { return __builtin_amdgcn_fmed3f(x, -448.0f, 448.0f); }
; DI void attn_unit_d8(unsigned char* lds, const AttnArgs& a) {
;     ...
;     const float r0 = 16.0f / lt0, r1 = 16.0f * a.lam / lt1;
;     float ss = 0.f;
; #pragma unroll
;     for (int d = 0; d < 2; ++d)
; #pragma unroll
;         for (int i = 0; i < 16; ++i) { const float v = o0[d][i] * r0 - o1[d][i] * r1; o0[d][i] = v; ss += v * v; }
;     ss += __shfl_xor(ss, 32);
;     const float rinv = rsqrtf(ss * (1.0f / 64.0f) + EPS) * a.oscale * CAT_SCALE;
;     f32x4 ggv[2][4];
; #pragma unroll
;     for (int d = 0; d < 2; ++d)
; #pragma unroll
;         for (int g = 0; g < 4; ++g) ggv[d][g] = *(const f32x4*)(a.subg + 32 * d + 8 * g + 4 * h);
;     asm volatile("" : "+v"(ggv[0][0]), "+v"(ggv[1][3]));
; #pragma unroll
;     for (int d = 0; d < 2; ++d)
; #pragma unroll
;         for (int g = 0; g < 4; ++g) { const f32x4 gg = ggv[d][g];
;             *(unsigned*)(op + 32 * d + 8 * g) = pk4_fp8(clamp448(o0[d][4 * g] * rinv * gg[0]), clamp448(o0[d][4 * g + 1] * rinv * gg[1]), clamp448(o0[d][4 * g + 2] * rinv * gg[2]), clamp448(o0[d][4 * g + 3] * rinv * gg[3])); }
	v_add_f32_e32 v26, v26, v27
	v_fmamk_f32 v26, v26, 0x3c800000, v215
	v_mul_f32_e32 v27, 0x4b800000, v26
	v_cmp_gt_f32_e32 vcc, s41, v26
	s_nop 1
	v_cndmask_b32_e32 v30, v26, v27, vcc
	global_load_dwordx4 v[26:29], v69, s[12:13] offset:384
	v_rsq_f32_e32 v32, v30
	v_lshlrev_b64 v[30:31], 10, v[180:181]
	v_lshl_add_u64 v[44:45], s[16:17], 0, v[30:31]
	v_lshl_add_u64 v[44:45], v[44:45], 0, v[178:179]
	v_mul_f32_e32 v30, 0x45800000, v32
	v_cndmask_b32_e32 v30, v32, v30, vcc
	v_mul_f32_e32 v48, v213, v30
	global_load_dwordx4 v[30:33], v69, s[12:13] offset:416
	v_mul_f32_e32 v48, 0x41800000, v48
	s_waitcnt vmcnt(5)
	v_mul_f32_e32 v49, v50, v48
	v_mul_f32_e32 v10, v10, v49
	v_mul_f32_e32 v49, v51, v48
	v_mul_f32_e32 v11, v11, v49
	v_mul_f32_e32 v49, v52, v48
	v_med3_f32 v10, v10, s42, v216
	v_med3_f32 v11, v11, s42, v216
	v_mul_f32_e32 v12, v12, v49
	s_nop 0
	v_cvt_pk_fp8_f32 v49, v10, v11
	v_mul_f32_e32 v10, v53, v48
	v_mul_f32_e32 v10, v13, v10
	v_med3_f32 v12, v12, s42, v216
	v_med3_f32 v10, v10, s42, v216
	v_cvt_pk_fp8_f32 v49, v12, v10 op_sel:[0,0,1]
	v_mul_f32_e32 v10, v54, v48
	v_mul_f32_e32 v6, v6, v10
	v_mul_f32_e32 v10, v55, v48
	v_mul_f32_e32 v7, v7, v10
	v_mul_f32_e32 v10, v56, v48
	v_med3_f32 v6, v6, s42, v216
	v_med3_f32 v7, v7, s42, v216
	v_mul_f32_e32 v8, v8, v10
	s_nop 0
	v_cvt_pk_fp8_f32 v10, v6, v7
	v_mul_f32_e32 v6, v57, v48
	v_mul_f32_e32 v6, v9, v6
	v_med3_f32 v8, v8, s42, v216
	v_med3_f32 v6, v6, s42, v216
	v_cvt_pk_fp8_f32 v10, v8, v6 op_sel:[0,0,1]
	v_add_co_u32_e32 v6, vcc, s43, v44
	v_lshl_add_u64 v[46:47], v[44:45], 0, s[14:15]
	s_nop 0
	v_addc_co_u32_e32 v7, vcc, 0, v45, vcc
	global_store_dword v[6:7], v49, off offset:768
	global_store_dword v[46:47], v10, off offset:8
	v_mul_f32_e32 v6, v58, v48
	v_mul_f32_e32 v7, v59, v48
	s_waitcnt vmcnt(6)
	v_mul_f32_e32 v6, v14, v6
	v_mul_f32_e32 v7, v15, v7
	v_med3_f32 v6, v6, s42, v216
	v_med3_f32 v7, v7, s42, v216
	s_nop 0
	v_cvt_pk_fp8_f32 v9, v6, v7
	v_mul_f32_e32 v8, v60, v48
	v_mul_f32_e32 v6, v61, v48
	v_mul_f32_e32 v8, v16, v8
	v_mul_f32_e32 v6, v17, v6
	v_med3_f32 v8, v8, s42, v216
	v_med3_f32 v6, v6, s42, v216
	v_cvt_pk_fp8_f32 v9, v8, v6 op_sel:[0,0,1]
	v_mul_f32_e32 v6, v62, v48
	v_mul_f32_e32 v7, v63, v48
	s_nop 0
	v_mul_f32_e32 v8, v64, v48
	s_nop 0
	s_waitcnt vmcnt(5)
	v_mul_f32_e32 v6, v18, v6
	v_mul_f32_e32 v7, v19, v7
	v_med3_f32 v6, v6, s42, v216
	v_med3_f32 v7, v7, s42, v216
	v_cvt_pk_fp8_f32 v10, v6, v7
	v_mul_f32_e32 v6, v65, v48
	v_mul_f32_e32 v8, v20, v8
	v_mul_f32_e32 v6, v21, v6
	v_med3_f32 v8, v8, s42, v216
	v_med3_f32 v6, v6, s42, v216
	v_cvt_pk_fp8_f32 v10, v8, v6 op_sel:[0,0,1]
	v_mul_f32_e32 v6, v70, v48
	v_mul_f32_e32 v7, v71, v48
	s_waitcnt vmcnt(3)
	v_mul_f32_e32 v6, v26, v6
	v_mul_f32_e32 v7, v27, v7
	v_med3_f32 v6, v6, s42, v216
	v_med3_f32 v7, v7, s42, v216
	v_cvt_pk_fp8_f32 v11, v6, v7
	v_mul_f32_e32 v8, v72, v48
	v_mul_f32_e32 v6, v73, v48
	v_mul_f32_e32 v8, v28, v8
	v_mul_f32_e32 v6, v29, v6
	v_med3_f32 v8, v8, s42, v216
	v_med3_f32 v6, v6, s42, v216
	v_cvt_pk_fp8_f32 v11, v8, v6 op_sel:[0,0,1]
	v_mul_f32_e32 v6, v74, v48
	v_mul_f32_e32 v7, v75, v48
	s_waitcnt vmcnt(2)
	v_mul_f32_e32 v6, v30, v6
	v_mul_f32_e32 v7, v31, v7
	v_med3_f32 v6, v6, s42, v216
	v_med3_f32 v7, v7, s42, v216
	s_nop 0
	v_cvt_pk_fp8_f32 v12, v6, v7
	v_mul_f32_e32 v8, v34, v48
	v_mul_f32_e32 v6, v35, v48
	v_mul_f32_e32 v8, v32, v8
	v_mul_f32_e32 v6, v33, v6
	v_med3_f32 v8, v8, s42, v216
	v_med3_f32 v6, v6, s42, v216
	v_cvt_pk_fp8_f32 v12, v8, v6 op_sel:[0,0,1]
	v_mul_f32_e32 v6, v36, v48
	v_mul_f32_e32 v7, v37, v48
	v_mul_f32_e32 v6, v22, v6
	v_mul_f32_e32 v7, v23, v7
	global_store_dword v[46:47], v9, off offset:16
	global_store_dword v[46:47], v10, off offset:24
	global_store_dword v[46:47], v11, off offset:32
	global_store_dword v[46:47], v12, off offset:40
	v_med3_f32 v6, v6, s42, v216
	v_med3_f32 v7, v7, s42, v216
	s_nop 0
	v_cvt_pk_fp8_f32 v9, v6, v7
	v_mul_f32_e32 v8, v38, v48
	v_mul_f32_e32 v6, v39, v48
	v_mul_f32_e32 v8, v24, v8
	v_mul_f32_e32 v6, v25, v6
	v_med3_f32 v8, v8, s42, v216
	v_med3_f32 v6, v6, s42, v216
	v_cvt_pk_fp8_f32 v9, v8, v6 op_sel:[0,0,1]
	v_mul_f32_e32 v6, v40, v48
	v_mul_f32_e32 v2, v2, v6
	v_mul_f32_e32 v6, v41, v48
	v_mul_f32_e32 v3, v3, v6
	v_mul_f32_e32 v6, v42, v48
	v_med3_f32 v2, v2, s42, v216
	v_med3_f32 v3, v3, s42, v216
	v_mul_f32_e32 v4, v4, v6
	s_nop 0
	v_cvt_pk_fp8_f32 v6, v2, v3
	v_mul_f32_e32 v2, v43, v48
	v_mul_f32_e32 v2, v5, v2
	v_med3_f32 v4, v4, s42, v216
	v_med3_f32 v2, v2, s42, v216
	v_cvt_pk_fp8_f32 v6, v4, v2 op_sel:[0,0,1]
	global_store_dword v[46:47], v9, off offset:48
	global_store_dword v[46:47], v6, off offset:56
	s_cbranch_scc0 .LBB0_1885
